# in-proj GEMM K loop: removed the compiler-added vmcnt(0) drain at the loop top (the template's counted vmcnt(8) waits already order the LDS-DMA stages; the out-proj instance has none)
# speedup vs baseline: 1.0239x; 1.0017x over previous
; #define PG8_STAGE_B(bufoff, gbase) do { if (FP8) { glds16s((gbase), vB[0], ldsb + (unsigned)(bufoff)); glds16s((gbase) + dB1, vB[0], ldsb + (unsigned)(bufoff) + 8192u); } \
;         else PG8_STAGE2(bufoff, gbase, vB[0], vB[1]); } while (0)
; #define PG8_STAGE_A(bufoff, gbase, hh, nx) do { if (FP8 && !GATHER) { glds16s((gbase) + (size_t)(hh) * dA2, vA[0][0], ldsb + (unsigned)(bufoff)); glds16s((gbase) + (size_t)(hh) * dA2 + dA1, vA[0][0], ldsb + (unsigned)(bufoff) + 8192u); } \
;         else PG8_STAGE2(bufoff, gbase, vA[hh][0], vA[hh][1]); } while (0)
; #define PG8_LDA(dst, b, h) do { if (FP8) { _Pragma("unroll") for (int m = 0; m < 4; ++m) dst##8[m] = PG8_LD8(lds + PG8_SA(b, h) + aoff + m * 2048); } else { \
;         _Pragma("unroll") for (int m = 0; m < 4; ++m) _Pragma("unroll") for (int k = 0; k < 2; ++k) dst[m][k] = *(const LAS bf16x8*)(lds + PG8_SA(b, h) + aoff + m * 2048 + k * 1024); } } while (0)
; #define PG8_MM(ai, bj, At, Bt) do { if (FP8) PG8_MMA8(ai, bj, At, Bt); else PG8_MMA(ai, bj, At, Bt); } while (0)
; #define PG8_WAIT_V(n) asm volatile("s_waitcnt vmcnt(" #n ")" ::: "memory")
; #define PG8_WAIT_L(n) asm volatile("s_waitcnt lgkmcnt(" #n ")" ::: "memory")
; #define PG8_BAR __builtin_amdgcn_s_barrier()
; template <bool GATHER, class Epi, class Sched, bool FP8 = false>
; DEV void gemm_phase(LAS char* lds, const Gemm g, const Sched& S, const Epi& E) {
;     ...
;         for (int t = 0; t < nt; t += 2) {
;             const bool last = (t == nt - 2), lastn = last && has_next;
;             const char* a1 = cA + (size_t)(t + 1) * kstep;
;             const char* a2 = last ? nA : cA + (size_t)(t + 2) * kstep; const char* b2 = last ? nB : cB + (size_t)(t + 2) * kstep;
;             const char* a3 = a2 + kstep; const char* b3 = b2 + kstep;
;             if (GATHER && lastn) PG8_GOFF(nxt, vA, 0);
;             PG8_LDB(B0, 0, 0); PG8_LDB(B1, 0, 1); PG8_SCHED; PG8_LDA(At, 0, 0); PG8_STAGE_A(PG8_SA(1, 1), a1, 1, false);
;             if (GATHER && lastn) PG8_GOFF(nxt, vA, 1);
;             PG8_WAIT_V(8); PG8_WAIT_L(0); PG8_BAR; PG8_MM(0, 0, At, B0); PG8_MM(0, 1, At, B1); PG8_BAR; PG8_SCHED;
;             PG8_LDA(At, 0, 1); PG8_STAGE_B(PG8_SB(0, 0), b2); PG8_STAGE_B(PG8_SB(0, 1), b2 + hstepB); PG8_STAGE_A(PG8_SA(0, 0), a2, 0, lastn);
;             PG8_WAIT_V(8); PG8_WAIT_L(0); PG8_BAR; PG8_MM(1, 0, At, B0); PG8_MM(1, 1, At, B1); PG8_BAR; PG8_SCHED;
.LBB0_287:
	s_add_i32 s48, s8, 2
	s_add_u32 s9, s6, 0x80
	s_addc_u32 s20, s7, 0
	s_add_i32 s49, 0, 0x10000
	s_cmp_eq_u32 s29, s8
	s_cselect_b32 s21, s97, s20
	s_cselect_b32 s20, s96, s9
	s_cselect_b32 s9, s44, s47
	s_cselect_b32 s8, s45, s46
	s_add_i32 s58, 0, 0x14000
	s_nop 0
	v_add_u32_e32 v50, s49, v183
	v_add_u32_e32 v174, s58, v183
	ds_read_b128 v[38:41], v50
	ds_read_b128 v[42:45], v50 offset:1024
	ds_read_b128 v[46:49], v50 offset:2048
	ds_read_b128 v[50:53], v50 offset:3072
	ds_read_b128 v[146:149], v174
	ds_read_b128 v[166:169], v174 offset:1024
	ds_read_b128 v[170:173], v174 offset:2048
	ds_read_b128 v[174:177], v174 offset:3072
	v_lshl_add_u64 v[180:181], s[6:7], 0, v[162:163]
	s_add_i32 m0, s28, 0xc000
	ds_read_b128 v[184:187], v190
	ds_read_b128 v[192:195], v190 offset:1024
	ds_read_b128 v[196:199], v190 offset:2048
	ds_read_b128 v[200:203], v190 offset:3072
	ds_read_b128 v[220:223], v190 offset:4096
	ds_read_b128 v[224:227], v190 offset:5120
	ds_read_b128 v[228:231], v190 offset:6144
	ds_read_b128 v[232:235], v190 offset:7168
	global_load_lds_dwordx4 v[180:181], off
	v_lshl_add_u64 v[180:181], s[6:7], 0, v[164:165]
	s_add_i32 m0, s28, 0xe000
	s_nop 0
	global_load_lds_dwordx4 v[180:181], off
	s_waitcnt vmcnt(8)
	s_waitcnt lgkmcnt(0)
	s_barrier
	s_setprio 1
	s_waitcnt lgkmcnt(0)
	v_mfma_f32_16x16x32_bf16 v[142:145], v[38:41], v[184:187], v[142:145]
	v_mfma_f32_16x16x32_bf16 v[138:141], v[46:49], v[184:187], v[138:141]
	v_mfma_f32_16x16x32_bf16 v[126:129], v[38:41], v[196:199], v[126:129]
	v_mfma_f32_16x16x32_bf16 v[122:125], v[46:49], v[196:199], v[122:125]
	v_mfma_f32_16x16x32_bf16 v[110:113], v[38:41], v[220:223], v[110:113]
	v_mfma_f32_16x16x32_bf16 v[106:109], v[46:49], v[220:223], v[106:109]
	v_mfma_f32_16x16x32_bf16 v[94:97], v[38:41], v[228:231], v[94:97]
	v_mfma_f32_16x16x32_bf16 v[90:93], v[46:49], v[228:231], v[90:93]
	v_mfma_f32_16x16x32_bf16 v[142:145], v[42:45], v[192:195], v[142:145]
	v_mfma_f32_16x16x32_bf16 v[138:141], v[50:53], v[192:195], v[138:141]
	v_mfma_f32_16x16x32_bf16 v[126:129], v[42:45], v[200:203], v[126:129]
	v_mfma_f32_16x16x32_bf16 v[122:125], v[50:53], v[200:203], v[122:125]
	v_mfma_f32_16x16x32_bf16 v[110:113], v[42:45], v[224:227], v[110:113]
	v_mfma_f32_16x16x32_bf16 v[106:109], v[50:53], v[224:227], v[106:109]
	v_mfma_f32_16x16x32_bf16 v[94:97], v[42:45], v[232:235], v[94:97]
	v_mfma_f32_16x16x32_bf16 v[90:93], v[50:53], v[232:235], v[90:93]
	s_setprio 0
	s_setprio 1
	v_mfma_f32_16x16x32_bf16 v[134:137], v[146:149], v[184:187], v[134:137]
	v_mfma_f32_16x16x32_bf16 v[130:133], v[170:173], v[184:187], v[130:133]
	v_mfma_f32_16x16x32_bf16 v[118:121], v[146:149], v[196:199], v[118:121]
	v_mfma_f32_16x16x32_bf16 v[114:117], v[170:173], v[196:199], v[114:117]
	v_mfma_f32_16x16x32_bf16 v[102:105], v[146:149], v[220:223], v[102:105]
	v_mfma_f32_16x16x32_bf16 v[98:101], v[170:173], v[220:223], v[98:101]
	v_mfma_f32_16x16x32_bf16 v[86:89], v[146:149], v[228:231], v[86:89]
	v_mfma_f32_16x16x32_bf16 v[82:85], v[170:173], v[228:231], v[82:85]
	v_mfma_f32_16x16x32_bf16 v[134:137], v[166:169], v[192:195], v[134:137]
	v_mfma_f32_16x16x32_bf16 v[130:133], v[174:177], v[192:195], v[130:133]
	v_mfma_f32_16x16x32_bf16 v[118:121], v[166:169], v[200:203], v[118:121]
	v_mfma_f32_16x16x32_bf16 v[114:117], v[174:177], v[200:203], v[114:117]
	v_mfma_f32_16x16x32_bf16 v[102:105], v[166:169], v[224:227], v[102:105]
	v_mfma_f32_16x16x32_bf16 v[98:101], v[174:177], v[224:227], v[98:101]
	v_mfma_f32_16x16x32_bf16 v[86:89], v[166:169], v[232:235], v[86:89]
	v_mfma_f32_16x16x32_bf16 v[82:85], v[174:177], v[232:235], v[82:85]
	s_setprio 0
	s_barrier
	s_add_i32 s49, s49, s50
	v_lshl_add_u64 v[180:181], s[8:9], 0, v[150:151]
	s_mov_b32 m0, s49
	ds_read_b128 v[184:187], v190 offset:16384
	ds_read_b128 v[192:195], v190 offset:17408
	ds_read_b128 v[196:199], v190 offset:18432
	ds_read_b128 v[200:203], v190 offset:19456
	ds_read_b128 v[220:223], v190 offset:20480
	ds_read_b128 v[224:227], v190 offset:21504
	ds_read_b128 v[228:231], v190 offset:22528
	ds_read_b128 v[232:235], v190 offset:23552
	global_load_lds_dwordx4 v[180:181], off
	s_add_i32 m0, s49, 0x2000
	s_add_u32 s54, s8, 0x10000
	v_lshl_add_u64 v[188:189], s[8:9], 0, v[156:157]
	s_addc_u32 s55, s9, 0
	s_add_i32 s49, s58, s50
	global_load_lds_dwordx4 v[188:189], off
	v_lshl_add_u64 v[204:205], s[54:55], 0, v[150:151]
	s_mov_b32 m0, s49
	v_lshl_add_u64 v[206:207], s[20:21], 0, v[158:159]
	global_load_lds_dwordx4 v[204:205], off
	v_lshl_add_u64 v[204:205], s[54:55], 0, v[156:157]
	s_add_i32 m0, s49, 0x2000
	s_nop 0
	global_load_lds_dwordx4 v[204:205], off
	v_lshl_add_u64 v[204:205], s[20:21], 0, v[152:153]
	s_mov_b32 m0, s28
	s_nop 0
	global_load_lds_dwordx4 v[204:205], off
	s_mov_b32 m0, s12
	s_nop 0
	global_load_lds_dwordx4 v[206:207], off
	s_waitcnt vmcnt(8)
	s_waitcnt lgkmcnt(0)
	s_barrier
; #define PG8_STAGE_B(bufoff, gbase) do { if (FP8) { glds16s((gbase), vB[0], ldsb + (unsigned)(bufoff)); glds16s((gbase) + dB1, vB[0], ldsb + (unsigned)(bufoff) + 8192u); } \
;         else PG8_STAGE2(bufoff, gbase, vB[0], vB[1]); } while (0)
; #define PG8_STAGE_A(bufoff, gbase, hh, nx) do { if (FP8 && !GATHER) { glds16s((gbase) + (size_t)(hh) * dA2, vA[0][0], ldsb + (unsigned)(bufoff)); glds16s((gbase) + (size_t)(hh) * dA2 + dA1, vA[0][0], ldsb + (unsigned)(bufoff) + 8192u); } \
;         else PG8_STAGE2(bufoff, gbase, vA[hh][0], vA[hh][1]); } while (0)
; #define PG8_LDA(dst, b, h) do { if (FP8) { _Pragma("unroll") for (int m = 0; m < 4; ++m) dst##8[m] = PG8_LD8(lds + PG8_SA(b, h) + aoff + m * 2048); } else { \
;         _Pragma("unroll") for (int m = 0; m < 4; ++m) _Pragma("unroll") for (int k = 0; k < 2; ++k) dst[m][k] = *(const LAS bf16x8*)(lds + PG8_SA(b, h) + aoff + m * 2048 + k * 1024); } } while (0)
; #define PG8_LDB(dst, b, h) do { if (FP8) { _Pragma("unroll") for (int n = 0; n < 2; ++n) dst##8[n] = PG8_LD8(lds + PG8_SB(b, h) + boff + n * 2048); } else { \
;         _Pragma("unroll") for (int n = 0; n < 2; ++n) _Pragma("unroll") for (int k = 0; k < 2; ++k) dst[n][k] = *(const LAS bf16x8*)(lds + PG8_SB(b, h) + boff + n * 2048 + k * 1024); } } while (0)
; #define PG8_MM(ai, bj, At, Bt) do { if (FP8) PG8_MMA8(ai, bj, At, Bt); else PG8_MMA(ai, bj, At, Bt); } while (0)
; #define PG8_WAIT_V(n) asm volatile("s_waitcnt vmcnt(" #n ")" ::: "memory")
; #define PG8_WAIT_L(n) asm volatile("s_waitcnt lgkmcnt(" #n ")" ::: "memory")
; #define PG8_BAR __builtin_amdgcn_s_barrier()
; #define PG8_SCHED __builtin_amdgcn_sched_barrier(0)
; template <bool GATHER, class Epi, class Sched, bool FP8 = false>
; DEV void gemm_phase(LAS char* lds, const Gemm g, const Sched& S, const Epi& E) {
;     ...
;             PG8_WAIT_V(8); PG8_WAIT_L(0); PG8_BAR; PG8_MM(1, 0, At, B0); PG8_MM(1, 1, At, B1); PG8_BAR; PG8_SCHED;
;             PG8_LDB(B0, 1, 0); PG8_LDB(B1, 1, 1); PG8_SCHED; PG8_LDA(At, 1, 0); PG8_STAGE_A(PG8_SA(0, 1), a2, 1, lastn);
;             PG8_WAIT_V(8); PG8_WAIT_L(0); PG8_BAR; PG8_MM(0, 0, At, B0); PG8_MM(0, 1, At, B1); PG8_BAR; PG8_SCHED;
;             PG8_LDA(At, 1, 1); PG8_STAGE_B(PG8_SB(1, 0), b3); PG8_STAGE_B(PG8_SB(1, 1), b3 + hstepB); PG8_STAGE_A(PG8_SA(1, 0), a3, 0, lastn);
	s_setprio 1
	s_waitcnt lgkmcnt(0)
	v_mfma_f32_16x16x32_bf16 v[78:81], v[38:41], v[184:187], v[78:81]
	v_mfma_f32_16x16x32_bf16 v[74:77], v[46:49], v[184:187], v[74:77]
	v_mfma_f32_16x16x32_bf16 v[62:65], v[38:41], v[196:199], v[62:65]
	v_mfma_f32_16x16x32_bf16 v[58:61], v[46:49], v[196:199], v[58:61]
	v_mfma_f32_16x16x32_bf16 v[30:33], v[38:41], v[220:223], v[30:33]
	v_mfma_f32_16x16x32_bf16 v[26:29], v[46:49], v[220:223], v[26:29]
	v_mfma_f32_16x16x32_bf16 v[14:17], v[38:41], v[228:231], v[14:17]
	v_mfma_f32_16x16x32_bf16 v[10:13], v[46:49], v[228:231], v[10:13]
	v_mfma_f32_16x16x32_bf16 v[78:81], v[42:45], v[192:195], v[78:81]
	v_mfma_f32_16x16x32_bf16 v[74:77], v[50:53], v[192:195], v[74:77]
	v_mfma_f32_16x16x32_bf16 v[62:65], v[42:45], v[200:203], v[62:65]
	v_mfma_f32_16x16x32_bf16 v[58:61], v[50:53], v[200:203], v[58:61]
	v_mfma_f32_16x16x32_bf16 v[30:33], v[42:45], v[224:227], v[30:33]
	v_mfma_f32_16x16x32_bf16 v[26:29], v[50:53], v[224:227], v[26:29]
	v_mfma_f32_16x16x32_bf16 v[14:17], v[42:45], v[232:235], v[14:17]
	v_mfma_f32_16x16x32_bf16 v[10:13], v[50:53], v[232:235], v[10:13]
	s_setprio 0
	s_setprio 1
	v_mfma_f32_16x16x32_bf16 v[34:37], v[170:173], v[196:199], v[34:37]
	v_mfma_f32_16x16x32_bf16 v[22:25], v[146:149], v[220:223], v[22:25]
	v_mfma_f32_16x16x32_bf16 v[18:21], v[170:173], v[220:223], v[18:21]
	v_mfma_f32_16x16x32_bf16 v[6:9], v[146:149], v[228:231], v[6:9]
	v_mfma_f32_16x16x32_bf16 v[2:5], v[170:173], v[228:231], v[2:5]
	v_mfma_f32_16x16x32_bf16 v[38:41], v[146:149], v[184:187], v[70:73]
	v_mfma_f32_16x16x32_bf16 v[42:45], v[170:173], v[184:187], v[66:69]
	v_mfma_f32_16x16x32_bf16 v[46:49], v[146:149], v[196:199], v[54:57]
	v_mfma_f32_16x16x32_bf16 v[34:37], v[174:177], v[200:203], v[34:37]
	v_mfma_f32_16x16x32_bf16 v[22:25], v[166:169], v[224:227], v[22:25]
	v_mfma_f32_16x16x32_bf16 v[18:21], v[174:177], v[224:227], v[18:21]
	v_mfma_f32_16x16x32_bf16 v[6:9], v[166:169], v[232:235], v[6:9]
	v_mfma_f32_16x16x32_bf16 v[2:5], v[174:177], v[232:235], v[2:5]
	v_mfma_f32_16x16x32_bf16 v[38:41], v[166:169], v[192:195], v[38:41]
	v_mfma_f32_16x16x32_bf16 v[42:45], v[174:177], v[192:195], v[42:45]
	v_mfma_f32_16x16x32_bf16 v[46:49], v[166:169], v[200:203], v[46:49]
	s_setprio 0
	s_barrier
	s_add_i32 s49, 0, 0x18000
	s_add_i32 s54, 0, 0x1c000
	v_add_u32_e32 v70, s49, v183
	v_add_u32_e32 v174, s54, v183
	ds_read_b128 v[50:53], v70
	ds_read_b128 v[54:57], v70 offset:1024
	ds_read_b128 v[66:69], v70 offset:2048
	ds_read_b128 v[70:73], v70 offset:3072
	ds_read_b128 v[146:149], v174
	ds_read_b128 v[166:169], v174 offset:1024
	ds_read_b128 v[170:173], v174 offset:2048
	ds_read_b128 v[174:177], v174 offset:3072
	s_mov_b32 m0, s13
	v_lshl_add_u64 v[210:211], s[20:21], 0, v[154:155]
	ds_read_b128 v[184:187], v190 offset:32768
	ds_read_b128 v[192:195], v190 offset:33792
	ds_read_b128 v[196:199], v190 offset:34816
	ds_read_b128 v[200:203], v190 offset:35840
	ds_read_b128 v[220:223], v190 offset:36864
	ds_read_b128 v[224:227], v190 offset:37888
	ds_read_b128 v[228:231], v190 offset:38912
	ds_read_b128 v[232:235], v190 offset:39936
	global_load_lds_dwordx4 v[210:211], off
	v_lshl_add_u64 v[210:211], s[20:21], 0, v[160:161]
	s_mov_b32 m0, s94
	s_nop 0
	global_load_lds_dwordx4 v[210:211], off
	s_waitcnt vmcnt(8)
	s_waitcnt lgkmcnt(0)
	s_barrier
	s_setprio 1
	s_waitcnt lgkmcnt(0)
	v_mfma_f32_16x16x32_bf16 v[142:145], v[50:53], v[184:187], v[142:145]
	v_mfma_f32_16x16x32_bf16 v[138:141], v[66:69], v[184:187], v[138:141]
	v_mfma_f32_16x16x32_bf16 v[126:129], v[50:53], v[196:199], v[126:129]
	v_mfma_f32_16x16x32_bf16 v[122:125], v[66:69], v[196:199], v[122:125]
	v_mfma_f32_16x16x32_bf16 v[110:113], v[50:53], v[220:223], v[110:113]
	v_mfma_f32_16x16x32_bf16 v[106:109], v[66:69], v[220:223], v[106:109]
	v_mfma_f32_16x16x32_bf16 v[94:97], v[50:53], v[228:231], v[94:97]
	v_mfma_f32_16x16x32_bf16 v[90:93], v[66:69], v[228:231], v[90:93]
	v_mfma_f32_16x16x32_bf16 v[142:145], v[54:57], v[192:195], v[142:145]
	v_mfma_f32_16x16x32_bf16 v[138:141], v[70:73], v[192:195], v[138:141]
	v_mfma_f32_16x16x32_bf16 v[126:129], v[54:57], v[200:203], v[126:129]
	v_mfma_f32_16x16x32_bf16 v[122:125], v[70:73], v[200:203], v[122:125]
	v_mfma_f32_16x16x32_bf16 v[110:113], v[54:57], v[224:227], v[110:113]
	v_mfma_f32_16x16x32_bf16 v[106:109], v[70:73], v[224:227], v[106:109]
	v_mfma_f32_16x16x32_bf16 v[94:97], v[54:57], v[232:235], v[94:97]
	v_mfma_f32_16x16x32_bf16 v[90:93], v[70:73], v[232:235], v[90:93]
	s_setprio 0
	s_setprio 1
	v_mfma_f32_16x16x32_bf16 v[134:137], v[146:149], v[184:187], v[134:137]
	v_mfma_f32_16x16x32_bf16 v[130:133], v[170:173], v[184:187], v[130:133]
	v_mfma_f32_16x16x32_bf16 v[118:121], v[146:149], v[196:199], v[118:121]
	v_mfma_f32_16x16x32_bf16 v[114:117], v[170:173], v[196:199], v[114:117]
	v_mfma_f32_16x16x32_bf16 v[102:105], v[146:149], v[220:223], v[102:105]
	v_mfma_f32_16x16x32_bf16 v[98:101], v[170:173], v[220:223], v[98:101]
	v_mfma_f32_16x16x32_bf16 v[86:89], v[146:149], v[228:231], v[86:89]
	v_mfma_f32_16x16x32_bf16 v[82:85], v[170:173], v[228:231], v[82:85]
	v_mfma_f32_16x16x32_bf16 v[134:137], v[166:169], v[192:195], v[134:137]
	v_mfma_f32_16x16x32_bf16 v[130:133], v[174:177], v[192:195], v[130:133]
	v_mfma_f32_16x16x32_bf16 v[118:121], v[166:169], v[200:203], v[118:121]
	v_mfma_f32_16x16x32_bf16 v[114:117], v[174:177], v[200:203], v[114:117]
	v_mfma_f32_16x16x32_bf16 v[102:105], v[166:169], v[224:227], v[102:105]
	v_mfma_f32_16x16x32_bf16 v[98:101], v[174:177], v[224:227], v[98:101]
	v_mfma_f32_16x16x32_bf16 v[86:89], v[166:169], v[232:235], v[86:89]
	v_mfma_f32_16x16x32_bf16 v[82:85], v[174:177], v[232:235], v[82:85]
	s_setprio 0
	s_barrier
; #define PG8_STAGE_B(bufoff, gbase) do { if (FP8) { glds16s((gbase), vB[0], ldsb + (unsigned)(bufoff)); glds16s((gbase) + dB1, vB[0], ldsb + (unsigned)(bufoff) + 8192u); } \
;         else PG8_STAGE2(bufoff, gbase, vB[0], vB[1]); } while (0)
; #define PG8_STAGE_A(bufoff, gbase, hh, nx) do { if (FP8 && !GATHER) { glds16s((gbase) + (size_t)(hh) * dA2, vA[0][0], ldsb + (unsigned)(bufoff)); glds16s((gbase) + (size_t)(hh) * dA2 + dA1, vA[0][0], ldsb + (unsigned)(bufoff) + 8192u); } \
;         else PG8_STAGE2(bufoff, gbase, vA[hh][0], vA[hh][1]); } while (0)
; #define PG8_LDA(dst, b, h) do { if (FP8) { _Pragma("unroll") for (int m = 0; m < 4; ++m) dst##8[m] = PG8_LD8(lds + PG8_SA(b, h) + aoff + m * 2048); } else { \
;         _Pragma("unroll") for (int m = 0; m < 4; ++m) _Pragma("unroll") for (int k = 0; k < 2; ++k) dst[m][k] = *(const LAS bf16x8*)(lds + PG8_SA(b, h) + aoff + m * 2048 + k * 1024); } } while (0)
; #define PG8_MM(ai, bj, At, Bt) do { if (FP8) PG8_MMA8(ai, bj, At, Bt); else PG8_MMA(ai, bj, At, Bt); } while (0)
; #define PG8_WAIT_V(n) asm volatile("s_waitcnt vmcnt(" #n ")" ::: "memory")
; #define PG8_WAIT_L(n) asm volatile("s_waitcnt lgkmcnt(" #n ")" ::: "memory")
; #define PG8_BAR __builtin_amdgcn_s_barrier()
; #define PG8_SCHED __builtin_amdgcn_sched_barrier(0)
; template <bool GATHER, class Epi, class Sched, bool FP8 = false>
; DEV void gemm_phase(LAS char* lds, const Gemm g, const Sched& S, const Epi& E) {
;     ...
;             PG8_LDA(At, 1, 1); PG8_STAGE_B(PG8_SB(1, 0), b3); PG8_STAGE_B(PG8_SB(1, 1), b3 + hstepB); PG8_STAGE_A(PG8_SA(1, 0), a3, 0, lastn);
;             PG8_WAIT_V(8); PG8_WAIT_L(0); PG8_BAR; PG8_MM(1, 0, At, B0); PG8_MM(1, 1, At, B1); PG8_BAR; PG8_SCHED;
;         }
	s_add_i32 s20, s49, s50
	v_lshl_add_u64 v[180:181], v[180:181], 0, s[92:93]
	s_mov_b32 m0, s20
	ds_read_b128 v[184:187], v190 offset:49152
	ds_read_b128 v[192:195], v190 offset:50176
	ds_read_b128 v[196:199], v190 offset:51200
	ds_read_b128 v[200:203], v190 offset:52224
	ds_read_b128 v[220:223], v190 offset:53248
	ds_read_b128 v[224:227], v190 offset:54272
	ds_read_b128 v[228:231], v190 offset:55296
	ds_read_b128 v[232:235], v190 offset:56320
	global_load_lds_dwordx4 v[180:181], off
	s_add_i32 m0, s20, 0x2000
	s_add_u32 s8, s8, 0x10080
	v_lshl_add_u64 v[180:181], v[188:189], 0, s[92:93]
	s_addc_u32 s9, s9, 0
	s_add_i32 s20, s54, s50
	global_load_lds_dwordx4 v[180:181], off
	v_lshl_add_u64 v[180:181], s[8:9], 0, v[150:151]
	s_mov_b32 m0, s20
	s_nop 0
	global_load_lds_dwordx4 v[180:181], off
	v_lshl_add_u64 v[180:181], s[8:9], 0, v[156:157]
	s_add_i32 m0, s20, 0x2000
	s_nop 0
	global_load_lds_dwordx4 v[180:181], off
	v_lshl_add_u64 v[180:181], v[204:205], 0, s[92:93]
	s_mov_b32 m0, s37
	s_nop 0
	global_load_lds_dwordx4 v[180:181], off
	v_lshl_add_u64 v[180:181], v[206:207], 0, s[92:93]
	s_mov_b32 m0, s17
	s_nop 0
	global_load_lds_dwordx4 v[180:181], off
	s_waitcnt vmcnt(8)
	s_waitcnt lgkmcnt(0)
	s_barrier
	s_setprio 1
	s_waitcnt lgkmcnt(0)
	v_mfma_f32_16x16x32_bf16 v[78:81], v[50:53], v[184:187], v[78:81]
	v_mfma_f32_16x16x32_bf16 v[74:77], v[66:69], v[184:187], v[74:77]
	v_mfma_f32_16x16x32_bf16 v[62:65], v[50:53], v[196:199], v[62:65]
	v_mfma_f32_16x16x32_bf16 v[58:61], v[66:69], v[196:199], v[58:61]
	v_mfma_f32_16x16x32_bf16 v[30:33], v[50:53], v[220:223], v[30:33]
	v_mfma_f32_16x16x32_bf16 v[26:29], v[66:69], v[220:223], v[26:29]
	v_mfma_f32_16x16x32_bf16 v[14:17], v[50:53], v[228:231], v[14:17]
	v_mfma_f32_16x16x32_bf16 v[10:13], v[66:69], v[228:231], v[10:13]
	v_mfma_f32_16x16x32_bf16 v[78:81], v[54:57], v[192:195], v[78:81]
	v_mfma_f32_16x16x32_bf16 v[74:77], v[70:73], v[192:195], v[74:77]
	v_mfma_f32_16x16x32_bf16 v[62:65], v[54:57], v[200:203], v[62:65]
	v_mfma_f32_16x16x32_bf16 v[58:61], v[70:73], v[200:203], v[58:61]
	v_mfma_f32_16x16x32_bf16 v[30:33], v[54:57], v[224:227], v[30:33]
	v_mfma_f32_16x16x32_bf16 v[26:29], v[70:73], v[224:227], v[26:29]
	v_mfma_f32_16x16x32_bf16 v[14:17], v[54:57], v[232:235], v[14:17]
	v_mfma_f32_16x16x32_bf16 v[10:13], v[70:73], v[232:235], v[10:13]
	s_setprio 0
	s_setprio 1
	v_mfma_f32_16x16x32_bf16 v[38:41], v[146:149], v[184:187], v[38:41]
	v_mfma_f32_16x16x32_bf16 v[70:73], v[166:169], v[192:195], v[38:41]
	v_mfma_f32_16x16x32_bf16 v[38:41], v[170:173], v[184:187], v[42:45]
	v_mfma_f32_16x16x32_bf16 v[66:69], v[174:177], v[192:195], v[38:41]
	v_mfma_f32_16x16x32_bf16 v[38:41], v[146:149], v[196:199], v[46:49]
	v_mfma_f32_16x16x32_bf16 v[34:37], v[170:173], v[196:199], v[34:37]
	v_mfma_f32_16x16x32_bf16 v[22:25], v[146:149], v[220:223], v[22:25]
	v_mfma_f32_16x16x32_bf16 v[18:21], v[170:173], v[220:223], v[18:21]
	v_mfma_f32_16x16x32_bf16 v[6:9], v[146:149], v[228:231], v[6:9]
	v_mfma_f32_16x16x32_bf16 v[2:5], v[170:173], v[228:231], v[2:5]
	v_mfma_f32_16x16x32_bf16 v[54:57], v[166:169], v[200:203], v[38:41]
	v_mfma_f32_16x16x32_bf16 v[34:37], v[174:177], v[200:203], v[34:37]
	v_mfma_f32_16x16x32_bf16 v[22:25], v[166:169], v[224:227], v[22:25]
	v_mfma_f32_16x16x32_bf16 v[18:21], v[174:177], v[224:227], v[18:21]
	v_mfma_f32_16x16x32_bf16 v[6:9], v[166:169], v[232:235], v[6:9]
	v_mfma_f32_16x16x32_bf16 v[2:5], v[174:177], v[232:235], v[2:5]
	s_setprio 0
	s_barrier
	s_add_u32 s6, s6, 0x100
	s_addc_u32 s7, s7, 0
	s_add_u32 s46, s46, 0x100
	s_addc_u32 s47, s47, 0
	s_cmp_ge_i32 s48, s18
	s_mov_b32 s8, s48
	s_cbranch_scc0 .LBB0_287
	s_and_b64 vcc, exec, s[70:71]
	s_cbranch_vccz .LBB0_290
